# stacked: conv balance (4 tiles) + exp1/exp2 preamble tables + ph_slots batched atomics
# speedup vs baseline: 1.0013x; 1.0013x over previous
.LBB0_3614:
	s_ashr_i32 s15, s14, 31
	s_lshl_b64 s[8:9], s[14:15], 2
	s_add_u32 s8, s33, s8
	s_addc_u32 s9, s36, s9
	v_readlane_b32 s12, v242, 0
	s_nop 0
	s_nop 0
